# aligned final + nt policy on the 32 final-output stores of the fused P10 epilogue
# baseline (speedup 1.0000x reference)
.LBB0_1376:
	s_or_b64 exec, exec, s[6:7]
	v_or_b32_e32 v2, s2, v194
	s_waitcnt lgkmcnt(0)
	v_ashrrev_i32_e32 v3, 31, v2
	s_barrier
	v_lshl_add_u64 v[6:7], v[2:3], 2, s[78:79]
	global_load_dwordx4 v[10:13], v[6:7], off offset:16
	global_load_dwordx4 v[14:17], v[6:7], off
	global_load_dwordx4 v[2:5], v[6:7], off offset:528
	s_nop 0
	global_load_dwordx4 v[6:9], v[6:7], off offset:512
	s_nop 0
	global_load_dword v19, v[60:61], off sc1
	global_load_dword v18, v[60:61], off offset:64 sc1
	global_load_dword v244, v[60:61], off offset:128 sc1
	global_load_dword v243, v[60:61], off offset:192 sc1
	global_load_dword v246, v[60:61], off offset:512 sc1
	global_load_dword v245, v[60:61], off offset:576 sc1
	global_load_dword v248, v[60:61], off offset:640 sc1
	global_load_dword v247, v[60:61], off offset:704 sc1
	s_mov_b32 s2, 0x358637bd
	v_mov_b64_e32 v[24:25], s[2:3]
	s_mov_b64 s[2:3], 0x20000
	s_waitcnt vmcnt(0)
	v_pk_fma_f32 v[18:19], v[18:19], s[36:37], v[24:25] op_sel_hi:[1,0,0]
	s_nop 0
	v_mul_f32_e32 v20, 0x4b800000, v19
	v_cmp_gt_f32_e64 s[6:7], s89, v19
	v_cmp_gt_f32_e32 vcc, s89, v18
	s_nop 0
	v_cndmask_b32_e64 v19, v19, v20, s[6:7]
	v_rsq_f32_e32 v19, v19
	s_nop 0
	v_mul_f32_e32 v20, 0x45800000, v19
	v_cndmask_b32_e64 v34, v19, v20, s[6:7]
	v_mul_f32_e32 v19, 0x4b800000, v18
	v_cndmask_b32_e32 v18, v18, v19, vcc
	v_rsq_f32_e32 v18, v18
	v_pk_mul_f32 v[32:33], v[66:67], v[34:35] op_sel_hi:[1,0]
	v_pk_mul_f32 v[36:37], v[68:69], v[34:35] op_sel_hi:[1,0]
	v_pk_mul_f32 v[40:41], v[128:129], v[34:35] op_sel_hi:[1,0]
	v_mul_f32_e32 v19, 0x45800000, v18
	v_cndmask_b32_e32 v26, v18, v19, vcc
	v_mov_b32_e32 v19, v244
	v_mov_b32_e32 v18, v243
	v_pk_mul_f32 v[38:39], v[16:17], v[36:37]
	v_pk_mul_f32 v[36:37], v[14:15], v[32:33]
	v_pk_mul_f32 v[32:33], v[126:127], v[34:35] op_sel_hi:[1,0]
	v_pk_mul_f32 v[42:43], v[12:13], v[40:41]
	v_pk_mul_f32 v[40:41], v[10:11], v[32:33]
	v_lshl_add_u64 v[32:33], v[58:59], 2, s[80:81]
	s_waitcnt vmcnt(0)
	v_pk_fma_f32 v[18:19], v[18:19], s[36:37], v[24:25] op_sel_hi:[1,0,0]
	s_nop 0
	v_mul_f32_e32 v20, 0x4b800000, v19
	v_cmp_gt_f32_e64 s[6:7], s89, v19
	v_cmp_gt_f32_e32 vcc, s89, v18
	s_nop 0
	v_cndmask_b32_e64 v19, v19, v20, s[6:7]
	v_rsq_f32_e32 v19, v19
	s_nop 0
	v_mul_f32_e32 v20, 0x45800000, v19
	v_cndmask_b32_e64 v30, v19, v20, s[6:7]
	v_mul_f32_e32 v19, 0x4b800000, v18
	v_cndmask_b32_e32 v18, v18, v19, vcc
	v_rsq_f32_e32 v18, v18
	s_nop 0
	v_mul_f32_e32 v19, 0x45800000, v18
	v_cndmask_b32_e32 v22, v18, v19, vcc
	v_mov_b32_e32 v19, v246
	v_mov_b32_e32 v18, v245
	s_waitcnt vmcnt(0)
	v_pk_fma_f32 v[18:19], v[18:19], s[36:37], v[24:25] op_sel_hi:[1,0,0]
	s_nop 0
	v_mul_f32_e32 v20, 0x4b800000, v19
	v_cmp_gt_f32_e64 s[6:7], s89, v19
	v_cmp_gt_f32_e32 vcc, s89, v18
	s_nop 0
	v_cndmask_b32_e64 v19, v19, v20, s[6:7]
	v_rsq_f32_e32 v19, v19
	s_nop 0
	v_mul_f32_e32 v20, 0x45800000, v19
	v_cndmask_b32_e64 v28, v19, v20, s[6:7]
	v_mul_f32_e32 v19, 0x4b800000, v18
	v_cndmask_b32_e32 v18, v18, v19, vcc
	v_rsq_f32_e32 v18, v18
	s_nop 0
	v_mul_f32_e32 v19, 0x45800000, v18
	v_cndmask_b32_e32 v20, v18, v19, vcc
	v_mov_b32_e32 v19, v248
	v_mov_b32_e32 v18, v247
	s_nop 0
	global_store_dwordx4 v[32:33], v[36:39], off nt
	global_store_dwordx4 v[32:33], v[40:43], off offset:16 nt
	s_waitcnt vmcnt(2)
	v_pk_fma_f32 v[18:19], v[18:19], s[36:37], v[24:25] op_sel_hi:[1,0,0]
	s_nop 0
	v_mul_f32_e32 v21, 0x4b800000, v19
	v_cmp_gt_f32_e64 s[6:7], s89, v19
	v_cmp_gt_f32_e32 vcc, s89, v18
	v_pk_mul_f32 v[36:37], v[98:99], v[34:35] op_sel_hi:[1,0]
	v_cndmask_b32_e64 v19, v19, v21, s[6:7]
	v_rsq_f32_e32 v19, v19
	v_pk_mul_f32 v[38:39], v[100:101], v[34:35] op_sel_hi:[1,0]
	v_pk_mul_f32 v[36:37], v[6:7], v[36:37]
	v_pk_mul_f32 v[38:39], v[8:9], v[38:39]
	v_mul_f32_e32 v21, 0x45800000, v19
	v_cndmask_b32_e64 v24, v19, v21, s[6:7]
	v_mul_f32_e32 v19, 0x4b800000, v18
	v_cndmask_b32_e32 v18, v18, v19, vcc
	v_rsq_f32_e32 v18, v18
	v_pk_mul_f32 v[40:41], v[94:95], v[34:35] op_sel_hi:[1,0]
	v_pk_mul_f32 v[34:35], v[96:97], v[34:35] op_sel_hi:[1,0]
	v_pk_mul_f32 v[40:41], v[2:3], v[40:41]
	v_mul_f32_e32 v19, 0x45800000, v18
	v_cndmask_b32_e32 v18, v18, v19, vcc
	v_pk_mul_f32 v[42:43], v[4:5], v[34:35]
	global_store_dwordx4 v[32:33], v[36:39], off offset:512 nt
	global_store_dwordx4 v[32:33], v[40:43], off offset:528 nt
	v_pk_mul_f32 v[34:35], v[122:123], v[26:27] op_sel_hi:[1,0]
	v_pk_mul_f32 v[36:37], v[124:125], v[26:27] op_sel_hi:[1,0]
	v_add_co_u32_e32 v44, vcc, s77, v32
	v_pk_mul_f32 v[36:37], v[16:17], v[36:37]
	v_pk_mul_f32 v[34:35], v[14:15], v[34:35]
	v_pk_mul_f32 v[38:39], v[118:119], v[26:27] op_sel_hi:[1,0]
	v_pk_mul_f32 v[40:41], v[120:121], v[26:27] op_sel_hi:[1,0]
	v_addc_co_u32_e32 v45, vcc, 0, v33, vcc
	v_pk_mul_f32 v[40:41], v[12:13], v[40:41]
	v_pk_mul_f32 v[38:39], v[10:11], v[38:39]
	v_lshl_add_u64 v[42:43], v[32:33], 0, s[2:3]
	global_store_dwordx4 v[44:45], v[34:37], off nt
	global_store_dwordx4 v[42:43], v[38:41], off offset:16 nt
	s_mov_b64 s[2:3], 0x40000
	v_pk_mul_f32 v[34:35], v[90:91], v[26:27] op_sel_hi:[1,0]
	v_pk_mul_f32 v[36:37], v[92:93], v[26:27] op_sel_hi:[1,0]
	v_pk_mul_f32 v[34:35], v[6:7], v[34:35]
	v_pk_mul_f32 v[36:37], v[8:9], v[36:37]
	v_pk_mul_f32 v[38:39], v[86:87], v[26:27] op_sel_hi:[1,0]
	v_pk_mul_f32 v[26:27], v[88:89], v[26:27] op_sel_hi:[1,0]
	v_pk_mul_f32 v[38:39], v[2:3], v[38:39]
	v_pk_mul_f32 v[40:41], v[4:5], v[26:27]
	global_store_dwordx4 v[42:43], v[34:37], off offset:512 nt
	global_store_dwordx4 v[42:43], v[38:41], off offset:528 nt
	v_pk_mul_f32 v[26:27], v[114:115], v[30:31] op_sel_hi:[1,0]
	v_pk_mul_f32 v[34:35], v[116:117], v[30:31] op_sel_hi:[1,0]
	v_pk_mul_f32 v[38:39], v[112:113], v[30:31] op_sel_hi:[1,0]
	v_pk_mul_f32 v[36:37], v[16:17], v[34:35]
	v_pk_mul_f32 v[34:35], v[14:15], v[26:27]
	v_pk_mul_f32 v[26:27], v[110:111], v[30:31] op_sel_hi:[1,0]
	v_add_co_u32_e32 v42, vcc, s90, v32
	v_pk_mul_f32 v[40:41], v[12:13], v[38:39]
	v_pk_mul_f32 v[38:39], v[10:11], v[26:27]
	v_addc_co_u32_e32 v43, vcc, 0, v33, vcc
	v_lshl_add_u64 v[26:27], v[32:33], 0, s[2:3]
	global_store_dwordx4 v[42:43], v[34:37], off nt
	global_store_dwordx4 v[26:27], v[38:41], off offset:16 nt
	s_nop 0
	v_pk_mul_f32 v[34:35], v[82:83], v[30:31] op_sel_hi:[1,0]
	v_pk_mul_f32 v[36:37], v[84:85], v[30:31] op_sel_hi:[1,0]
	v_pk_mul_f32 v[38:39], v[78:79], v[30:31] op_sel_hi:[1,0]
	v_pk_mul_f32 v[30:31], v[80:81], v[30:31] op_sel_hi:[1,0]
	v_pk_mul_f32 v[36:37], v[8:9], v[36:37]
	v_pk_mul_f32 v[34:35], v[6:7], v[34:35]
	v_pk_mul_f32 v[40:41], v[4:5], v[30:31]
	v_pk_mul_f32 v[30:31], v[108:109], v[22:23] op_sel_hi:[1,0]
	v_pk_mul_f32 v[38:39], v[2:3], v[38:39]
	global_store_dwordx4 v[26:27], v[34:37], off offset:512 nt
	global_store_dwordx4 v[26:27], v[38:41], off offset:528 nt
	v_pk_mul_f32 v[26:27], v[106:107], v[22:23] op_sel_hi:[1,0]
	v_pk_mul_f32 v[36:37], v[16:17], v[30:31]
	v_pk_mul_f32 v[30:31], v[104:105], v[22:23] op_sel_hi:[1,0]
	v_pk_mul_f32 v[34:35], v[14:15], v[26:27]
	v_pk_mul_f32 v[40:41], v[12:13], v[30:31]
	v_add_co_u32_e32 v30, vcc, s91, v32
	v_pk_mul_f32 v[26:27], v[102:103], v[22:23] op_sel_hi:[1,0]
	s_nop 0
	v_addc_co_u32_e32 v31, vcc, 0, v33, vcc
	v_pk_mul_f32 v[38:39], v[10:11], v[26:27]
	v_lshl_add_u64 v[26:27], v[32:33], 0, s[40:41]
	global_store_dwordx4 v[30:31], v[34:37], off nt
	global_store_dwordx4 v[26:27], v[38:41], off offset:16 nt
	v_pk_mul_f32 v[30:31], v[74:75], v[22:23] op_sel_hi:[1,0]
	v_pk_mul_f32 v[34:35], v[76:77], v[22:23] op_sel_hi:[1,0]
	s_nop 0
	v_pk_mul_f32 v[36:37], v[8:9], v[34:35]
	v_pk_mul_f32 v[34:35], v[6:7], v[30:31]
	v_pk_mul_f32 v[30:31], v[70:71], v[22:23] op_sel_hi:[1,0]
	v_pk_mul_f32 v[22:23], v[72:73], v[22:23] op_sel_hi:[1,0]
	v_pk_mul_f32 v[38:39], v[2:3], v[30:31]
	v_pk_mul_f32 v[40:41], v[4:5], v[22:23]
	global_store_dwordx4 v[26:27], v[34:37], off offset:512 nt
	global_store_dwordx4 v[26:27], v[38:41], off offset:528 nt
	v_pk_mul_f32 v[26:27], v[192:193], v[28:29] op_sel_hi:[1,0]
	v_pk_mul_f32 v[22:23], v[190:191], v[28:29] op_sel_hi:[1,0]
	v_pk_mul_f32 v[36:37], v[16:17], v[26:27]
	v_pk_mul_f32 v[26:27], v[188:189], v[28:29] op_sel_hi:[1,0]
	v_pk_mul_f32 v[34:35], v[14:15], v[22:23]
	v_pk_mul_f32 v[40:41], v[12:13], v[26:27]
	v_add_co_u32_e32 v26, vcc, s92, v32
	v_pk_mul_f32 v[22:23], v[186:187], v[28:29] op_sel_hi:[1,0]
	s_nop 0
	v_addc_co_u32_e32 v27, vcc, 0, v33, vcc
	v_pk_mul_f32 v[38:39], v[10:11], v[22:23]
	v_lshl_add_u64 v[22:23], v[32:33], 0, s[42:43]
	global_store_dwordx4 v[26:27], v[34:37], off nt
	global_store_dwordx4 v[22:23], v[38:41], off offset:16 nt
	v_pk_mul_f32 v[26:27], v[158:159], v[28:29] op_sel_hi:[1,0]
	v_pk_mul_f32 v[30:31], v[160:161], v[28:29] op_sel_hi:[1,0]
	v_pk_mul_f32 v[34:35], v[6:7], v[26:27]
	v_pk_mul_f32 v[26:27], v[154:155], v[28:29] op_sel_hi:[1,0]
	v_pk_mul_f32 v[36:37], v[8:9], v[30:31]
	v_pk_mul_f32 v[28:29], v[156:157], v[28:29] op_sel_hi:[1,0]
	v_pk_mul_f32 v[26:27], v[2:3], v[26:27]
	v_pk_mul_f32 v[28:29], v[4:5], v[28:29]
	global_store_dwordx4 v[22:23], v[34:37], off offset:512 nt
	global_store_dwordx4 v[22:23], v[26:29], off offset:528 nt
	v_pk_mul_f32 v[22:23], v[182:183], v[20:21] op_sel_hi:[1,0]
	v_pk_mul_f32 v[30:31], v[180:181], v[20:21] op_sel_hi:[1,0]
	v_pk_mul_f32 v[26:27], v[184:185], v[20:21] op_sel_hi:[1,0]
	v_pk_mul_f32 v[36:37], v[12:13], v[30:31]
	v_pk_mul_f32 v[28:29], v[16:17], v[26:27]
	v_pk_mul_f32 v[26:27], v[14:15], v[22:23]
	v_pk_mul_f32 v[22:23], v[178:179], v[20:21] op_sel_hi:[1,0]
	v_lshl_add_u64 v[30:31], v[32:33], 0, s[44:45]
	v_pk_mul_f32 v[34:35], v[10:11], v[22:23]
	v_add_co_u32_e32 v22, vcc, s93, v32
	s_nop 1
	v_addc_co_u32_e32 v23, vcc, 0, v33, vcc
	global_store_dwordx4 v[22:23], v[26:29], off nt
	global_store_dwordx4 v[30:31], v[34:37], off offset:16 nt
	v_pk_mul_f32 v[22:23], v[150:151], v[20:21] op_sel_hi:[1,0]
	v_pk_mul_f32 v[26:27], v[152:153], v[20:21] op_sel_hi:[1,0]
	v_pk_mul_f32 v[34:35], v[146:147], v[20:21] op_sel_hi:[1,0]
	v_pk_mul_f32 v[20:21], v[148:149], v[20:21] op_sel_hi:[1,0]
	v_pk_mul_f32 v[28:29], v[8:9], v[26:27]
	v_pk_mul_f32 v[26:27], v[6:7], v[22:23]
	v_pk_mul_f32 v[22:23], v[4:5], v[20:21]
	v_pk_mul_f32 v[20:21], v[2:3], v[34:35]
	global_store_dwordx4 v[30:31], v[26:29], off offset:512 nt
	global_store_dwordx4 v[30:31], v[20:23], off offset:528 nt
	v_add_co_u32_e32 v34, vcc, s94, v32
	s_nop 0
	v_pk_mul_f32 v[20:21], v[174:175], v[24:25] op_sel_hi:[1,0]
	v_pk_mul_f32 v[22:23], v[176:177], v[24:25] op_sel_hi:[1,0]
	v_pk_mul_f32 v[20:21], v[14:15], v[20:21]
	v_pk_mul_f32 v[22:23], v[16:17], v[22:23]
	v_pk_mul_f32 v[26:27], v[170:171], v[24:25] op_sel_hi:[1,0]
	v_pk_mul_f32 v[28:29], v[172:173], v[24:25] op_sel_hi:[1,0]
	v_addc_co_u32_e32 v35, vcc, 0, v33, vcc
	v_pk_mul_f32 v[28:29], v[12:13], v[28:29]
	v_pk_mul_f32 v[26:27], v[10:11], v[26:27]
	v_lshl_add_u64 v[30:31], v[32:33], 0, s[46:47]
	global_store_dwordx4 v[34:35], v[20:23], off nt
	global_store_dwordx4 v[30:31], v[26:29], off offset:16 nt
	s_nop 0
	v_pk_mul_f32 v[20:21], v[142:143], v[24:25] op_sel_hi:[1,0]
	v_pk_mul_f32 v[22:23], v[144:145], v[24:25] op_sel_hi:[1,0]
	v_pk_mul_f32 v[20:21], v[6:7], v[20:21]
	v_pk_mul_f32 v[22:23], v[8:9], v[22:23]
	v_pk_mul_f32 v[28:29], v[138:139], v[24:25] op_sel_hi:[1,0]
	v_pk_mul_f32 v[24:25], v[140:141], v[24:25] op_sel_hi:[1,0]
	s_nop 0
	v_pk_mul_f32 v[26:27], v[4:5], v[24:25]
	v_pk_mul_f32 v[24:25], v[2:3], v[28:29]
	global_store_dwordx4 v[30:31], v[20:23], off offset:512 nt
	global_store_dwordx4 v[30:31], v[24:27], off offset:528 nt
	s_nop 0
	v_pk_mul_f32 v[22:23], v[168:169], v[18:19] op_sel_hi:[1,0]
	v_pk_mul_f32 v[20:21], v[166:167], v[18:19] op_sel_hi:[1,0]
	v_pk_mul_f32 v[16:17], v[16:17], v[22:23]
	v_pk_mul_f32 v[22:23], v[164:165], v[18:19] op_sel_hi:[1,0]
	v_pk_mul_f32 v[14:15], v[14:15], v[20:21]
	v_pk_mul_f32 v[20:21], v[162:163], v[18:19] op_sel_hi:[1,0]
	v_pk_mul_f32 v[12:13], v[12:13], v[22:23]
	v_add_co_u32_e32 v22, vcc, s95, v32
	v_pk_mul_f32 v[10:11], v[10:11], v[20:21]
	s_nop 0
	v_addc_co_u32_e32 v23, vcc, 0, v33, vcc
	v_lshl_add_u64 v[20:21], v[32:33], 0, s[48:49]
	global_store_dwordx4 v[22:23], v[14:17], off nt
	global_store_dwordx4 v[20:21], v[10:13], off offset:16 nt
	s_andn2_b64 vcc, exec, s[22:23]
	s_nop 0
	v_pk_mul_f32 v[10:11], v[134:135], v[18:19] op_sel_hi:[1,0]
	v_pk_mul_f32 v[12:13], v[136:137], v[18:19] op_sel_hi:[1,0]
	v_pk_mul_f32 v[6:7], v[6:7], v[10:11]
	v_pk_mul_f32 v[8:9], v[8:9], v[12:13]
	v_pk_mul_f32 v[10:11], v[130:131], v[18:19] op_sel_hi:[1,0]
	v_pk_mul_f32 v[12:13], v[132:133], v[18:19] op_sel_hi:[1,0]
	v_pk_mul_f32 v[2:3], v[2:3], v[10:11]
	v_pk_mul_f32 v[4:5], v[4:5], v[12:13]
	global_store_dwordx4 v[20:21], v[6:9], off offset:512 nt
	global_store_dwordx4 v[20:21], v[2:5], off offset:528 nt
	s_cbranch_vccnz .LBB0_1388
	s_mov_b64 s[22:23], 0
	s_cmp_gt_i32 s28, 0x3ffffffd
	s_mov_b32 s3, s20
	s_mov_b32 s6, s62
	s_cbranch_scc1 .LBB0_1384
	s_ashr_i32 s29, s28, 31
	s_lshl_b64 s[2:3], s[28:29], 8
	s_add_u32 s2, s2, s87
	s_addc_u32 s3, s3, s39
	s_add_u32 s2, s2, 0x200
	s_addc_u32 s3, s3, 0
	v_cmp_gt_i64_e32 vcc, s[2:3], v[212:213]
	s_mov_b32 s6, s62
	s_mov_b32 s3, s20
	s_cbranch_vccnz .LBB0_1384
	s_ashr_i32 s3, s2, 31
	s_lshr_b32 s3, s3, 29
	s_add_i32 s6, s2, s3
	s_and_b32 s3, s6, -8
	s_sub_i32 s7, s2, s3
	s_cmp_gt_i32 s7, -1
	s_mov_b64 s[2:3], -1
	s_cbranch_scc0 .LBB0_1381
	s_lshl_b32 s18, s7, 6
	s_mov_b64 s[2:3], 0
